# DeltaNet recurrence: read-once operand tile loads marked nt (keeps the attention K/V working set in cache)
# speedup vs baseline: 1.0089x; 1.0089x over previous
.LBB0_799:
	s_ashr_i32 s4, s16, 1
	s_lshl_b32 s20, s4, 6
	s_and_b32 s17, s4, 3
	s_and_b32 s4, s20, 0xffffff00
	s_or_b32 s14, s4, s17
	s_ashr_i32 s15, s14, 31
	s_lshl_b64 s[4:5], s[14:15], 13
	v_readlane_b32 s6, v253, 22
	v_lshl_add_u64 v[20:21], v[134:135], 0, s[4:5]
	v_readlane_b32 s7, v253, 23
	s_add_u32 s4, s6, s4
	s_addc_u32 s5, s7, s5
	s_lshl_b32 s6, s16, 11
	s_and_b32 s6, s6, 0x800
	v_or_b32_e32 v36, s6, v132
	v_lshlrev_b32_e32 v2, 1, v132
	v_mov_b32_e32 v143, v3
	v_mov_b32_e32 v37, v3
	v_lshlrev_b32_e32 v36, 1, v36
	v_lshl_add_u64 v[16:17], v[20:21], 0, v[2:3]
	v_lshl_add_u64 v[32:33], v[20:21], 0, v[142:143]
	v_mov_b32_e32 v145, v3
	v_lshl_add_u64 v[38:39], s[4:5], 0, v[36:37]
	global_load_dwordx4 v[4:7], v[16:17], off nt
	global_load_dwordx4 v[8:11], v[16:17], off offset:32 nt
	global_load_dwordx4 v[12:15], v[16:17], off offset:64 nt
	v_lshl_add_u64 v[38:39], v[38:39], 0, v[144:145]
	global_load_dwordx4 v[16:19], v[16:17], off offset:96 nt
	s_nop 0
	global_load_dwordx4 v[20:23], v[32:33], off nt
	global_load_dwordx4 v[24:27], v[32:33], off offset:32 nt
	global_load_dwordx4 v[28:31], v[32:33], off offset:64 nt
	s_nop 0
	global_load_dwordx4 v[32:35], v[32:33], off offset:96 nt
	s_nop 0
	global_load_dwordx2 v[158:159], v[38:39], off nt
	global_load_dwordx2 v[154:155], v[38:39], off offset:16 nt
	global_load_dwordx2 v[152:153], v[38:39], off offset:32 nt
	global_load_dwordx2 v[150:151], v[38:39], off offset:48 nt
	global_load_dwordx2 v[164:165], v[38:39], off offset:64 nt
	global_load_dwordx2 v[162:163], v[38:39], off offset:80 nt
	global_load_dwordx2 v[160:161], v[38:39], off offset:96 nt
	global_load_dwordx2 v[156:157], v[38:39], off offset:112 nt
	v_lshl_add_u64 v[146:147], v[138:139], 0, v[36:37]
	v_lshl_add_u64 v[148:149], v[140:141], 0, v[36:37]
	s_mov_b32 s15, 0
	s_waitcnt vmcnt(0)
	v_cndmask_b32_e32 v38, v4, v6, vcc
	ds_bpermute_b32 v38, v166, v38
	s_waitcnt lgkmcnt(0)
	v_cndmask_b32_e32 v92, v38, v4, vcc
	v_mov_b32_e32 v4, 0
	v_mov_b32_e32 v93, v5
	v_mov_b32_e32 v95, v7
	s_nop 3
	v_permlane32_swap_b32_e32 v93, v95
	s_nop 1
	v_cndmask_b32_e32 v94, v6, v38, vcc
	s_waitcnt lgkmcnt(0)
	v_mov_b64_e32 v[76:77], v[8:9]
	v_mov_b64_e32 v[78:79], v[10:11]
	s_nop 3
	v_permlane32_swap_b32_e32 v77, v79
	v_permlane32_swap_b32_e32 v76, v78
	s_nop 1
	s_waitcnt lgkmcnt(0)
	v_mov_b64_e32 v[84:85], v[12:13]
	v_mov_b64_e32 v[86:87], v[14:15]
	s_nop 3
	v_permlane32_swap_b32_e32 v85, v87
	v_permlane32_swap_b32_e32 v84, v86
	s_nop 1
	s_waitcnt lgkmcnt(0)
	v_mov_b64_e32 v[68:69], v[16:17]
	v_mov_b64_e32 v[70:71], v[18:19]
	s_nop 3
	v_permlane32_swap_b32_e32 v69, v71
	v_permlane32_swap_b32_e32 v68, v70
	s_nop 1
	s_waitcnt lgkmcnt(0)
	v_mov_b64_e32 v[96:97], v[20:21]
	v_mov_b64_e32 v[98:99], v[22:23]
	s_nop 3
	v_permlane32_swap_b32_e32 v97, v99
	v_permlane32_swap_b32_e32 v96, v98
	s_nop 1
	s_waitcnt lgkmcnt(0)
	v_mov_b64_e32 v[80:81], v[24:25]
	v_mov_b64_e32 v[82:83], v[26:27]
	s_nop 3
	v_permlane32_swap_b32_e32 v81, v83
	v_permlane32_swap_b32_e32 v80, v82
	s_nop 1
	s_waitcnt lgkmcnt(0)
	v_mov_b64_e32 v[88:89], v[28:29]
	v_mov_b64_e32 v[90:91], v[30:31]
	s_nop 3
	v_permlane32_swap_b32_e32 v89, v91
	v_permlane32_swap_b32_e32 v88, v90
	s_nop 1
	s_waitcnt lgkmcnt(0)
	v_mov_b64_e32 v[72:73], v[32:33]
	v_mov_b64_e32 v[74:75], v[34:35]
	s_nop 3
	v_permlane32_swap_b32_e32 v73, v75
	v_permlane32_swap_b32_e32 v72, v74
	s_nop 1
	v_mov_b32_e32 v5, v4
	v_mov_b32_e32 v6, v4
	v_mov_b32_e32 v7, v4
	v_mov_b32_e32 v8, v4
	v_mov_b32_e32 v9, v4
	v_mov_b32_e32 v10, v4
	v_mov_b32_e32 v11, v4
	v_mov_b32_e32 v12, v4
	v_mov_b32_e32 v13, v4
	v_mov_b32_e32 v14, v4
	v_mov_b32_e32 v15, v4
	v_mov_b32_e32 v16, v4
	v_mov_b32_e32 v17, v4
	v_mov_b32_e32 v18, v4
	v_mov_b32_e32 v19, v4
	v_mov_b32_e32 v20, v4
	v_mov_b32_e32 v21, v4
	v_mov_b32_e32 v22, v4
	v_mov_b32_e32 v23, v4
	v_mov_b32_e32 v24, v4
	v_mov_b32_e32 v25, v4
	v_mov_b32_e32 v26, v4
	v_mov_b32_e32 v27, v4
	v_mov_b32_e32 v28, v4
	v_mov_b32_e32 v29, v4
	v_mov_b32_e32 v30, v4
	v_mov_b32_e32 v31, v4
	v_mov_b32_e32 v32, v4
	v_mov_b32_e32 v33, v4
	v_mov_b32_e32 v34, v4
	v_mov_b32_e32 v35, v4
.LBB0_800:
	v_lshlrev_b32_e32 v36, 16, v158
	v_and_b32_e32 v37, 0xffff0000, v158
	v_lshlrev_b32_e32 v38, 16, v159
	v_and_b32_e32 v39, 0xffff0000, v159
	v_lshlrev_b32_e32 v40, 16, v154
	v_and_b32_e32 v41, 0xffff0000, v154
	v_lshlrev_b32_e32 v42, 16, v155
	v_and_b32_e32 v43, 0xffff0000, v155
	v_lshlrev_b32_e32 v44, 16, v152
	v_and_b32_e32 v45, 0xffff0000, v152
	v_lshlrev_b32_e32 v46, 16, v153
	v_and_b32_e32 v47, 0xffff0000, v153
	v_lshlrev_b32_e32 v48, 16, v150
	v_and_b32_e32 v49, 0xffff0000, v150
	v_lshlrev_b32_e32 v50, 16, v151
	v_and_b32_e32 v51, 0xffff0000, v151
	v_cvt_pk_bf16_f32 v116, -v20, -v21
	v_cvt_pk_bf16_f32 v117, -v22, -v23
	v_cvt_pk_bf16_f32 v118, -v24, -v25
	v_cvt_pk_bf16_f32 v119, -v26, -v27
	v_lshlrev_b32_e32 v52, 16, v164
	v_and_b32_e32 v53, 0xffff0000, v164
	v_mfma_f32_32x32x16_bf16 v[36:51], v[92:95], v[116:119], v[36:51]
	v_lshlrev_b32_e32 v54, 16, v165
	v_and_b32_e32 v55, 0xffff0000, v165
	v_lshlrev_b32_e32 v56, 16, v162
	v_and_b32_e32 v57, 0xffff0000, v162
	v_lshlrev_b32_e32 v58, 16, v163
	v_and_b32_e32 v59, 0xffff0000, v163
	v_lshlrev_b32_e32 v60, 16, v160
	v_and_b32_e32 v61, 0xffff0000, v160
	v_lshlrev_b32_e32 v62, 16, v161
	v_and_b32_e32 v63, 0xffff0000, v161
	v_lshlrev_b32_e32 v64, 16, v156
	v_and_b32_e32 v65, 0xffff0000, v156
	v_lshlrev_b32_e32 v66, 16, v157
	v_and_b32_e32 v67, 0xffff0000, v157
	s_add_i32 s18, s14, s15
	s_ashr_i32 s19, s18, 31
	v_mfma_f32_32x32x16_bf16 v[52:67], v[96:99], v[116:119], v[52:67]
	s_lshl_b64 s[4:5], s[18:19], 2
	v_cvt_pk_bf16_f32 v120, -v4, -v5
	v_cvt_pk_bf16_f32 v121, -v6, -v7
	v_cvt_pk_bf16_f32 v122, -v8, -v9
	v_cvt_pk_bf16_f32 v123, -v10, -v11
	s_add_u32 s8, s12, s4
	s_addc_u32 s9, s13, s5
	s_lshl_b64 s[6:7], s[18:19], 13
	v_mfma_f32_32x32x16_bf16 v[36:51], v[84:87], v[120:123], v[36:51]
	v_lshl_add_u64 v[96:97], v[136:137], 0, s[6:7]
	v_cvt_pk_bf16_f32 v124, -v28, -v29
	v_cvt_pk_bf16_f32 v125, -v30, -v31
	v_lshl_add_u64 v[150:151], v[96:97], 0, v[2:3]
	v_mfma_f32_32x32x16_bf16 v[52:67], v[88:91], v[120:123], v[52:67]
	v_cvt_pk_bf16_f32 v126, -v32, -v33
	global_load_dword v204, v3, s[8:9]
	v_lshl_add_u64 v[152:153], v[96:97], 0, v[142:143]
	global_load_dwordx4 v[96:99], v[150:151], off nt
	global_load_dwordx4 v[116:119], v[150:151], off offset:32 nt
	s_add_i32 s4, s18, 4
	s_ashr_i32 s5, s4, 31
	s_lshl_b64 s[4:5], s[4:5], 13
	v_cvt_pk_bf16_f32 v127, -v34, -v35
	global_load_dwordx4 v[84:87], v[152:153], off nt
	global_load_dwordx4 v[128:131], v[152:153], off offset:32 nt
	global_load_dwordx4 v[168:171], v[150:151], off offset:64 nt
	global_load_dwordx4 v[172:175], v[150:151], off offset:96 nt
	global_load_dwordx4 v[176:179], v[152:153], off offset:64 nt
	global_load_dwordx4 v[180:183], v[152:153], off offset:96 nt
	v_lshl_add_u64 v[150:151], v[134:135], 0, s[4:5]
	v_lshl_add_u64 v[88:89], v[146:147], 0, s[4:5]
	v_cvt_pk_bf16_f32 v92, -v12, -v13
	v_cvt_pk_bf16_f32 v93, -v14, -v15
	v_cvt_pk_bf16_f32 v94, -v16, -v17
	v_cvt_pk_bf16_f32 v95, -v18, -v19
	v_lshl_add_u64 v[120:121], v[150:151], 0, v[2:3]
	v_lshl_add_u64 v[196:197], v[150:151], 0, v[142:143]
	global_load_dwordx2 v[158:159], v[88:89], off nt
	global_load_dwordx2 v[154:155], v[88:89], off offset:16 nt
	global_load_dwordx2 v[152:153], v[88:89], off offset:32 nt
	v_mfma_f32_32x32x16_bf16 v[36:51], v[76:79], v[124:127], v[36:51]
	global_load_dwordx2 v[150:151], v[88:89], off offset:48 nt
	global_load_dwordx2 v[164:165], v[88:89], off offset:64 nt
	global_load_dwordx2 v[162:163], v[88:89], off offset:80 nt
	global_load_dwordx2 v[160:161], v[88:89], off offset:96 nt
	global_load_dwordx2 v[156:157], v[88:89], off offset:112 nt
	global_load_dwordx4 v[76:79], v[120:121], off nt
	s_nop 0
	global_load_dwordx4 v[88:91], v[120:121], off offset:32 nt
	v_cvt_pk_bf16_f32 v100, v20, v21
	v_cvt_pk_bf16_f32 v101, v22, v23
	v_cvt_pk_bf16_f32 v102, v4, v5
	v_cvt_pk_bf16_f32 v103, v6, v7
	v_cvt_pk_bf16_f32 v104, v24, v25
	v_cvt_pk_bf16_f32 v105, v26, v27
	v_mfma_f32_32x32x16_bf16 v[52:67], v[80:83], v[124:127], v[52:67]
	global_load_dwordx4 v[80:83], v[120:121], off offset:64 nt
	s_nop 0
	global_load_dwordx4 v[120:123], v[120:121], off offset:96 nt
	s_nop 0
	global_load_dwordx4 v[184:187], v[196:197], off nt
	global_load_dwordx4 v[188:191], v[196:197], off offset:32 nt
	global_load_dwordx4 v[192:195], v[196:197], off offset:64 nt
	s_nop 0
	global_load_dwordx4 v[196:199], v[196:197], off offset:96 nt
	v_lshl_add_u64 v[206:207], v[148:149], 0, s[6:7]
	v_cvt_pk_bf16_f32 v106, v8, v9
	v_cvt_pk_bf16_f32 v107, v10, v11
	v_cvt_pk_bf16_f32 v108, v28, v29
	v_cvt_pk_bf16_f32 v109, v30, v31
	v_cvt_pk_bf16_f32 v110, v12, v13
	v_mfma_f32_32x32x16_bf16 v[36:51], v[68:71], v[92:95], v[36:51]
	v_cvt_pk_bf16_f32 v111, v14, v15
	v_cvt_pk_bf16_f32 v112, v32, v33
	v_cvt_pk_bf16_f32 v113, v34, v35
	v_cvt_pk_bf16_f32 v114, v16, v17
	v_cvt_pk_bf16_f32 v115, v18, v19
	global_store_dwordx2 v[206:207], v[100:101], off
	global_store_dwordx2 v[206:207], v[102:103], off offset:64
	global_store_dwordx2 v[206:207], v[104:105], off offset:16
	global_store_dwordx2 v[206:207], v[106:107], off offset:80
	global_store_dwordx2 v[206:207], v[108:109], off offset:32
	global_store_dwordx2 v[206:207], v[110:111], off offset:96
	global_store_dwordx2 v[206:207], v[112:113], off offset:48
	global_store_dwordx2 v[206:207], v[114:115], off offset:112
	v_mfma_f32_32x32x16_bf16 v[52:67], v[72:75], v[92:95], v[52:67]
	v_cvt_pk_bf16_f32 v36, v36, v37
	v_cvt_pk_bf16_f32 v37, v38, v39
	v_cvt_pk_bf16_f32 v39, v42, v43
	v_cvt_pk_bf16_f32 v42, v48, v49
	v_cvt_pk_bf16_f32 v38, v40, v41
	v_cvt_pk_bf16_f32 v40, v44, v45
	v_cvt_pk_bf16_f32 v43, v50, v51
	s_nop 4
	v_cvt_pk_bf16_f32 v52, v52, v53
	v_cvt_pk_bf16_f32 v53, v54, v55
	v_cvt_pk_bf16_f32 v54, v56, v57
	v_cvt_pk_bf16_f32 v44, v60, v61
	v_cvt_pk_bf16_f32 v45, v62, v63
	v_cvt_pk_bf16_f32 v41, v46, v47
	v_cvt_pk_bf16_f32 v46, v64, v65
	v_lshl_add_u64 v[208:209], v[146:147], 0, s[6:7]
	v_cvt_pk_bf16_f32 v55, v58, v59
	v_cvt_pk_bf16_f32 v47, v66, v67
	global_store_dwordx2 v[208:209], v[36:37], off
	global_store_dwordx2 v[208:209], v[52:53], off offset:64
	global_store_dwordx2 v[208:209], v[38:39], off offset:16
	global_store_dwordx2 v[208:209], v[54:55], off offset:80
	global_store_dwordx2 v[208:209], v[40:41], off offset:32
	global_store_dwordx2 v[208:209], v[44:45], off offset:96
	global_store_dwordx2 v[208:209], v[42:43], off offset:48
	global_store_dwordx2 v[208:209], v[46:47], off offset:112
	s_add_i32 s15, s15, 4
	s_cmpk_lg_i32 s15, 0xfc
	s_waitcnt vmcnt(40)
	v_pk_mul_f32 v[34:35], v[34:35], v[204:205] op_sel_hi:[1,0]
	s_waitcnt vmcnt(39)
	s_waitcnt vmcnt(38)
	v_pk_mul_f32 v[32:33], v[32:33], v[204:205] op_sel_hi:[1,0]
	v_pk_mul_f32 v[30:31], v[30:31], v[204:205] op_sel_hi:[1,0]
	v_pk_mul_f32 v[28:29], v[28:29], v[204:205] op_sel_hi:[1,0]
	s_waitcnt vmcnt(37)
	s_waitcnt vmcnt(35)
	s_waitcnt vmcnt(34)
	v_pk_mul_f32 v[26:27], v[26:27], v[204:205] op_sel_hi:[1,0]
	v_pk_mul_f32 v[24:25], v[24:25], v[204:205] op_sel_hi:[1,0]
	v_pk_mul_f32 v[22:23], v[22:23], v[204:205] op_sel_hi:[1,0]
	s_waitcnt vmcnt(23)
	v_pk_mul_f32 v[20:21], v[20:21], v[204:205] op_sel_hi:[1,0]
	v_pk_mul_f32 v[18:19], v[18:19], v[204:205] op_sel_hi:[1,0]
	v_pk_mul_f32 v[16:17], v[16:17], v[204:205] op_sel_hi:[1,0]
	s_waitcnt vmcnt(20)
	v_cndmask_b32_e32 v60, v120, v122, vcc
	v_cndmask_b32_e32 v61, v121, v123, vcc
	s_waitcnt vmcnt(19)
	v_cndmask_b32_e32 v62, v184, v186, vcc
	v_cndmask_b32_e32 v63, v185, v187, vcc
	v_pk_mul_f32 v[14:15], v[14:15], v[204:205] op_sel_hi:[1,0]
	v_pk_mul_f32 v[12:13], v[12:13], v[204:205] op_sel_hi:[1,0]
	v_pk_mul_f32 v[10:11], v[10:11], v[204:205] op_sel_hi:[1,0]
	v_pk_mul_f32 v[8:9], v[8:9], v[204:205] op_sel_hi:[1,0]
	v_pk_mul_f32 v[6:7], v[6:7], v[204:205] op_sel_hi:[1,0]
	v_pk_mul_f32 v[4:5], v[4:5], v[204:205] op_sel_hi:[1,0]
	ds_bpermute_b32 v145, v166, v60
	ds_bpermute_b32 v167, v166, v61
	ds_bpermute_b32 v203, v166, v62
	ds_bpermute_b32 v204, v166, v63
	s_waitcnt lgkmcnt(0)
	v_mov_b64_e32 v[48:49], v[96:97]
	v_mov_b64_e32 v[50:51], v[98:99]
	s_nop 3
	v_permlane32_swap_b32_e32 v49, v51
	v_permlane32_swap_b32_e32 v48, v50
	s_nop 1
	s_waitcnt lgkmcnt(0)
	v_mov_b64_e32 v[60:61], v[84:85]
	v_mov_b64_e32 v[62:63], v[86:87]
	s_nop 3
	v_permlane32_swap_b32_e32 v61, v63
	v_permlane32_swap_b32_e32 v60, v62
	s_nop 1
	v_mfma_f32_32x32x16_bf16 v[20:35], v[48:51], v[36:39], v[20:35]
	s_waitcnt lgkmcnt(0)
	v_mov_b64_e32 v[48:49], v[168:169]
	v_mov_b64_e32 v[50:51], v[170:171]
	s_nop 3
	v_permlane32_swap_b32_e32 v49, v51
	v_permlane32_swap_b32_e32 v48, v50
	s_nop 1
	v_mfma_f32_32x32x16_bf16 v[4:19], v[60:63], v[36:39], v[4:19]
	s_waitcnt lgkmcnt(0)
	v_mov_b64_e32 v[36:37], v[176:177]
	v_mov_b64_e32 v[38:39], v[178:179]
	s_nop 3
	v_permlane32_swap_b32_e32 v37, v39
	v_permlane32_swap_b32_e32 v36, v38
	s_nop 1
	v_mfma_f32_32x32x16_bf16 v[20:35], v[48:51], v[52:55], v[20:35]
	s_waitcnt vmcnt(18)
	v_mfma_f32_32x32x16_bf16 v[4:19], v[36:39], v[52:55], v[4:19]
	s_waitcnt vmcnt(17)
	v_mov_b64_e32 v[56:57], v[116:117]
	v_mov_b64_e32 v[58:59], v[118:119]
	s_nop 3
	v_permlane32_swap_b32_e32 v57, v59
	v_permlane32_swap_b32_e32 v56, v58
	s_nop 1
	s_waitcnt lgkmcnt(0)
	v_mov_b64_e32 v[64:65], v[128:129]
	v_mov_b64_e32 v[66:67], v[130:131]
	s_nop 3
	v_permlane32_swap_b32_e32 v65, v67
	v_permlane32_swap_b32_e32 v64, v66
	s_nop 1
	v_mfma_f32_32x32x16_bf16 v[20:35], v[56:59], v[40:43], v[20:35]
	v_mov_b64_e32 v[68:69], v[172:173]
	v_mov_b64_e32 v[70:71], v[174:175]
	s_nop 3
	v_permlane32_swap_b32_e32 v69, v71
	v_permlane32_swap_b32_e32 v68, v70
	s_nop 1
	s_waitcnt lgkmcnt(0)
	v_mov_b64_e32 v[60:61], v[180:181]
	v_mov_b64_e32 v[62:63], v[182:183]
	s_nop 3
	v_permlane32_swap_b32_e32 v61, v63
	v_permlane32_swap_b32_e32 v60, v62
	s_nop 1
	v_mfma_f32_32x32x16_bf16 v[4:19], v[64:67], v[40:43], v[4:19]
	s_waitcnt vmcnt(16)
	v_mov_b64_e32 v[128:129], v[76:77]
	v_mov_b64_e32 v[130:131], v[78:79]
	s_nop 3
	v_permlane32_swap_b32_e32 v129, v131
	v_permlane32_swap_b32_e32 v128, v130
	s_nop 1
	v_mfma_f32_32x32x16_bf16 v[20:35], v[68:71], v[44:47], v[20:35]
	s_waitcnt lgkmcnt(0)
	v_mov_b64_e32 v[112:113], v[88:89]
	v_mov_b64_e32 v[114:115], v[90:91]
	s_nop 3
	v_permlane32_swap_b32_e32 v113, v115
	v_permlane32_swap_b32_e32 v112, v114
	s_nop 1
	s_waitcnt lgkmcnt(0)
	v_mov_b64_e32 v[124:125], v[80:81]
	v_mov_b64_e32 v[126:127], v[82:83]
	s_nop 3
	v_permlane32_swap_b32_e32 v125, v127
	v_permlane32_swap_b32_e32 v124, v126
	s_nop 1
	v_mfma_f32_32x32x16_bf16 v[4:19], v[60:63], v[44:47], v[4:19]
	v_cndmask_b32_e32 v109, v167, v121, vcc
	v_cndmask_b32_e32 v108, v145, v120, vcc
	v_cndmask_b32_e32 v121, v204, v185, vcc
	v_cndmask_b32_e32 v120, v203, v184, vcc
	s_waitcnt lgkmcnt(0)
	v_mov_b64_e32 v[104:105], v[188:189]
	v_mov_b64_e32 v[106:107], v[190:191]
	s_nop 3
	v_permlane32_swap_b32_e32 v105, v107
	v_permlane32_swap_b32_e32 v104, v106
	s_nop 1
	s_waitcnt lgkmcnt(0)
	v_mov_b64_e32 v[116:117], v[192:193]
	v_mov_b64_e32 v[118:119], v[194:195]
	s_nop 3
	v_permlane32_swap_b32_e32 v117, v119
	v_permlane32_swap_b32_e32 v116, v118
	s_nop 1
	s_waitcnt lgkmcnt(0)
	v_mov_b64_e32 v[100:101], v[196:197]
	v_mov_b64_e32 v[102:103], v[198:199]
	s_nop 3
	v_permlane32_swap_b32_e32 v101, v103
	v_permlane32_swap_b32_e32 v100, v102
	s_nop 1
	v_cndmask_b32_e32 v111, v123, v167, vcc
	v_cndmask_b32_e32 v110, v122, v145, vcc
	v_cndmask_b32_e32 v123, v187, v204, vcc
	v_cndmask_b32_e32 v122, v186, v203, vcc
	v_mov_b64_e32 v[72:73], v[100:101]
	v_mov_b64_e32 v[88:89], v[116:117]
	v_mov_b64_e32 v[80:81], v[104:105]
	v_mov_b64_e32 v[96:97], v[120:121]
	v_mov_b64_e32 v[68:69], v[108:109]
	v_mov_b64_e32 v[84:85], v[124:125]
	v_mov_b64_e32 v[76:77], v[112:113]
	v_mov_b64_e32 v[92:93], v[128:129]
	v_mov_b64_e32 v[74:75], v[102:103]
	v_mov_b64_e32 v[90:91], v[118:119]
	v_mov_b64_e32 v[82:83], v[106:107]
	v_mov_b64_e32 v[98:99], v[122:123]
	v_mov_b64_e32 v[70:71], v[110:111]
	v_mov_b64_e32 v[86:87], v[126:127]
	v_mov_b64_e32 v[78:79], v[114:115]
	v_mov_b64_e32 v[94:95], v[130:131]
	s_cbranch_scc1 .LBB0_800
	v_cvt_pk_bf16_f32 v70, v20, v21
	v_cvt_pk_bf16_f32 v20, -v20, -v21
	v_cvt_pk_bf16_f32 v71, v22, v23
	v_cvt_pk_bf16_f32 v21, -v22, -v23
	v_cvt_pk_bf16_f32 v22, -v24, -v25
	v_lshlrev_b32_e32 v52, 16, v158
	v_and_b32_e32 v53, 0xffff0000, v158
	v_lshlrev_b32_e32 v54, 16, v159
	v_and_b32_e32 v55, 0xffff0000, v159
	v_lshlrev_b32_e32 v56, 16, v154
	v_and_b32_e32 v57, 0xffff0000, v154
	v_lshlrev_b32_e32 v58, 16, v155
	v_and_b32_e32 v59, 0xffff0000, v155
	v_lshlrev_b32_e32 v60, 16, v152
	v_and_b32_e32 v61, 0xffff0000, v152
	v_lshlrev_b32_e32 v62, 16, v153
	v_and_b32_e32 v63, 0xffff0000, v153
	v_lshlrev_b32_e32 v64, 16, v150
	v_and_b32_e32 v65, 0xffff0000, v150
	v_lshlrev_b32_e32 v66, 16, v151
	v_and_b32_e32 v67, 0xffff0000, v151
	v_cvt_pk_bf16_f32 v23, -v26, -v27
	v_lshlrev_b32_e32 v36, 16, v164
	v_and_b32_e32 v37, 0xffff0000, v164
	v_lshlrev_b32_e32 v38, 16, v165
	v_and_b32_e32 v39, 0xffff0000, v165
	v_lshlrev_b32_e32 v40, 16, v162
	v_and_b32_e32 v41, 0xffff0000, v162
	v_lshlrev_b32_e32 v42, 16, v163
	v_and_b32_e32 v43, 0xffff0000, v163
	v_lshlrev_b32_e32 v44, 16, v160
	v_and_b32_e32 v45, 0xffff0000, v160
	v_lshlrev_b32_e32 v46, 16, v161
	v_and_b32_e32 v47, 0xffff0000, v161
	v_lshlrev_b32_e32 v48, 16, v156
	v_and_b32_e32 v49, 0xffff0000, v156
	v_lshlrev_b32_e32 v50, 16, v157
	v_and_b32_e32 v51, 0xffff0000, v157
	v_mfma_f32_32x32x16_bf16 v[52:67], v[128:131], v[20:23], v[52:67]
	v_cvt_pk_bf16_f32 v72, v4, v5
	v_cvt_pk_bf16_f32 v4, -v4, -v5
	v_cvt_pk_bf16_f32 v73, v6, v7
	v_mfma_f32_32x32x16_bf16 v[36:51], v[120:123], v[20:23], v[36:51]
	v_cvt_pk_bf16_f32 v5, -v6, -v7
	v_cvt_pk_bf16_f32 v6, -v8, -v9
	v_cvt_pk_bf16_f32 v7, -v10, -v11
	s_or_b32 s4, s20, s17
	v_mfma_f32_32x32x16_bf16 v[52:67], v[124:127], v[4:7], v[52:67]
	s_or_b32 s4, s4, 0xfc
	s_ashr_i32 s5, s4, 31
	s_lshl_b64 s[14:15], s[4:5], 13
	v_lshl_add_u64 v[68:69], v[148:149], 0, s[14:15]
	global_store_dwordx2 v[68:69], v[70:71], off
	global_store_dwordx2 v[68:69], v[72:73], off offset:64
	v_cvt_pk_bf16_f32 v72, v8, v9
	v_mfma_f32_32x32x16_bf16 v[36:51], v[116:119], v[4:7], v[36:51]
	v_cvt_pk_bf16_f32 v4, -v28, -v29
	v_cvt_pk_bf16_f32 v5, -v30, -v31
	v_cvt_pk_bf16_f32 v6, -v32, -v33
	v_cvt_pk_bf16_f32 v7, -v34, -v35
	v_cvt_pk_bf16_f32 v8, -v12, -v13
	v_mfma_f32_32x32x16_bf16 v[52:67], v[112:115], v[4:7], v[52:67]
	v_cvt_pk_bf16_f32 v73, v10, v11
	v_cvt_pk_bf16_f32 v9, -v14, -v15
	v_cvt_pk_bf16_f32 v10, -v16, -v17
	v_mfma_f32_32x32x16_bf16 v[36:51], v[104:107], v[4:7], v[36:51]
	v_xor_b32_e32 v2, 0x80000000, v18
	v_xor_b32_e32 v11, 0x80000000, v19
	v_cvt_pk_bf16_f32 v11, v2, v11
	v_cvt_pk_bf16_f32 v70, v24, v25
	v_cvt_pk_bf16_f32 v71, v26, v27
	global_store_dwordx2 v[68:69], v[70:71], off offset:16
	global_store_dwordx2 v[68:69], v[72:73], off offset:80
	v_cvt_pk_bf16_f32 v70, v28, v29
	v_mfma_f32_32x32x16_bf16 v[52:67], v[108:111], v[8:11], v[52:67]
	v_cvt_pk_bf16_f32 v71, v30, v31
	v_cvt_pk_bf16_f32 v72, v12, v13
	v_cvt_pk_bf16_f32 v73, v14, v15
	global_store_dwordx2 v[68:69], v[70:71], off offset:32
	global_store_dwordx2 v[68:69], v[72:73], off offset:96
	v_cvt_pk_bf16_f32 v70, v32, v33
	v_cvt_pk_bf16_f32 v71, v34, v35
	v_lshl_add_u64 v[4:5], v[146:147], 0, s[14:15]
	v_mfma_f32_32x32x16_bf16 v[36:51], v[100:103], v[8:11], v[36:51]
	s_nop 2
	v_cvt_pk_bf16_f32 v6, v52, v53
	v_cvt_pk_bf16_f32 v7, v54, v55
	v_cvt_pk_bf16_f32 v72, v16, v17
	v_cvt_pk_bf16_f32 v73, v18, v19
	global_store_dwordx2 v[68:69], v[70:71], off offset:48
	global_store_dwordx2 v[68:69], v[72:73], off offset:112
	s_add_i32 s16, s16, s54
	s_cmp_lt_i32 s16, 64
	s_nop 0
	v_cvt_pk_bf16_f32 v8, v36, v37
	v_cvt_pk_bf16_f32 v9, v38, v39
	global_store_dwordx2 v[4:5], v[6:7], off
	global_store_dwordx2 v[4:5], v[8:9], off offset:64
	v_cvt_pk_bf16_f32 v6, v56, v57
	v_cvt_pk_bf16_f32 v7, v58, v59
	v_cvt_pk_bf16_f32 v8, v40, v41
	v_cvt_pk_bf16_f32 v9, v42, v43
	global_store_dwordx2 v[4:5], v[6:7], off offset:16
	global_store_dwordx2 v[4:5], v[8:9], off offset:80
	v_cvt_pk_bf16_f32 v6, v60, v61
	v_cvt_pk_bf16_f32 v7, v62, v63
	v_cvt_pk_bf16_f32 v8, v44, v45
	v_cvt_pk_bf16_f32 v9, v46, v47
	global_store_dwordx2 v[4:5], v[6:7], off offset:32
	global_store_dwordx2 v[4:5], v[8:9], off offset:96
	v_cvt_pk_bf16_f32 v6, v64, v65
	v_cvt_pk_bf16_f32 v7, v66, v67
	v_cvt_pk_bf16_f32 v8, v48, v49
	v_cvt_pk_bf16_f32 v9, v50, v51
	global_store_dwordx2 v[4:5], v[6:7], off offset:48
	global_store_dwordx2 v[4:5], v[8:9], off offset:112
	s_cbranch_scc1 .LBB0_799
